# speedup vs baseline: 1.0108x; 1.0072x over previous
.Lk2_stg_done:
	v_lshlrev_b32_e32 v18, 4, v1
	s_waitcnt lgkmcnt(0)
	s_barrier
	v_add_u32_e32 v19, 0xe240, v18
	ds_read_b128 v[150:153], v18 offset:57920
	ds_read_b128 v[146:149], v18 offset:58944
	ds_read_b128 v[142:145], v18 offset:59968
	ds_read_b128 v[138:141], v18 offset:60992
	ds_read_b128 v[134:137], v18 offset:62016
	ds_read_b128 v[130:133], v18 offset:63040
	ds_read_b128 v[126:129], v18 offset:64064
	ds_read_b128 v[122:125], v18 offset:65088
	ds_read_b128 v[118:121], v19 offset:8192
	ds_read_b128 v[114:117], v19 offset:9216
	ds_read_b128 v[110:113], v19 offset:10240
	ds_read_b128 v[106:109], v19 offset:11264
	ds_read_b128 v[102:105], v19 offset:12288
	ds_read_b128 v[98:101], v19 offset:13312
	ds_read_b128 v[94:97], v19 offset:14336
	ds_read_b128 v[90:93], v19 offset:15360
	ds_read_b128 v[86:89], v19 offset:16384
	ds_read_b128 v[82:85], v19 offset:17408
	v_lshl_or_b32 v166, v163, 5, v165
	v_mul_u32_u24_e32 v18, 0xe39, v166
	v_lshrrev_b32_e32 v168, 16, v18
	s_movk_i32 s4, 0xffee
	v_mad_i32_i24 v169, v168, s4, v166
	v_min_u32_e32 v19, 0x43, v166
	v_mad_u32_u24 v18, v168, 20, v169
	v_or_b32_e32 v165, 0x100, v19
	s_movk_i32 s2, 0xc0
	v_mul_lo_u32 v18, v18, s8
	v_mul_u32_u24_e32 v19, 0xe39, v165
	v_cmp_gt_u32_e32 vcc, s2, v0
	s_movk_i32 s2, 0xbf
	v_lshrrev_b32_e32 v167, 16, v19
	v_cmp_lt_u32_e64 s[2:3], s2, v0
	v_add_u32_e32 v171, v18, v162
	s_and_saveexec_b64 s[6:7], s[2:3]
	s_xor_b64 s[2:3], exec, s[6:7]
	s_cbranch_execz .LBB1_2
	ds_read_b128 v[34:37], v171
	ds_read_b128 v[38:41], v171 offset:32
	ds_read_b128 v[42:45], v171 offset:80
	ds_read_b128 v[46:49], v171 offset:112
	ds_read_b128 v[172:175], v171 offset:160
	ds_read_b128 v[176:179], v171 offset:192
	ds_read_b128 v[180:183], v171 offset:1600
	ds_read_b128 v[184:187], v171 offset:1632
	ds_read_b128 v[188:191], v171 offset:1680
	s_waitcnt vmcnt(0) lgkmcnt(8)
	v_mfma_f32_32x32x16_f16 v[18:33], v[150:153], v[34:37], v[2:17]
	s_waitcnt lgkmcnt(7)
	v_mfma_f32_32x32x16_f16 v[18:33], v[146:149], v[38:41], v[18:33]
	ds_read_b128 v[34:37], v171 offset:1712
	global_load_dwordx4 v[66:69], v210, s[10:11]
	s_waitcnt lgkmcnt(7)
	v_mfma_f32_32x32x16_f16 v[18:33], v[142:145], v[42:45], v[18:33]
	ds_read_b128 v[38:41], v171 offset:1760
	global_load_dwordx4 v[50:53], v210, s[10:11] offset:16
	s_waitcnt lgkmcnt(7)
	v_mfma_f32_32x32x16_f16 v[18:33], v[138:141], v[46:49], v[18:33]
	ds_read_b128 v[42:45], v171 offset:1792
	global_load_dwordx2 v[156:157], v210, s[10:11] offset:32
	s_waitcnt lgkmcnt(7)
	v_mfma_f32_32x32x16_f16 v[18:33], v[134:137], v[172:175], v[18:33]
	ds_read_b128 v[46:49], v171 offset:3200
	global_load_dwordx4 v[70:73], v210, s[10:11] offset:320
	s_waitcnt lgkmcnt(7)
	v_mfma_f32_32x32x16_f16 v[18:33], v[130:133], v[176:179], v[18:33]
	ds_read_b128 v[172:175], v171 offset:3232
	global_load_dwordx4 v[54:57], v210, s[10:11] offset:336
	s_waitcnt lgkmcnt(7)
	v_mfma_f32_32x32x16_f16 v[18:33], v[126:129], v[180:183], v[18:33]
	ds_read_b128 v[176:179], v171 offset:3280
	global_load_dwordx2 v[154:155], v210, s[10:11] offset:352
	s_waitcnt lgkmcnt(7)
	v_mfma_f32_32x32x16_f16 v[18:33], v[122:125], v[184:187], v[18:33]
	ds_read_b128 v[180:183], v171 offset:3312
	global_load_dwordx4 v[74:77], v210, s[10:11] offset:640
	s_waitcnt lgkmcnt(7)
	v_mfma_f32_32x32x16_f16 v[18:33], v[118:121], v[188:191], v[18:33]
	ds_read_b128 v[184:187], v171 offset:3360
	global_load_dwordx4 v[58:61], v210, s[10:11] offset:656
	s_waitcnt lgkmcnt(7)
	v_mfma_f32_32x32x16_f16 v[18:33], v[114:117], v[34:37], v[18:33]
	ds_read_b128 v[188:191], v171 offset:3392
	global_load_dwordx2 v[160:161], v210, s[10:11] offset:672
	s_waitcnt lgkmcnt(7)
	v_mfma_f32_32x32x16_f16 v[18:33], v[110:113], v[38:41], v[18:33]
	global_load_dwordx4 v[78:81], v210, s[10:11] offset:960
	s_waitcnt lgkmcnt(6)
	v_mfma_f32_32x32x16_f16 v[18:33], v[106:109], v[42:45], v[18:33]
	global_load_dwordx4 v[62:65], v210, s[10:11] offset:976
	s_waitcnt lgkmcnt(5)
	v_mfma_f32_32x32x16_f16 v[18:33], v[102:105], v[46:49], v[18:33]
	global_load_dwordx2 v[158:159], v210, s[10:11] offset:992
	s_waitcnt lgkmcnt(4)
	v_mfma_f32_32x32x16_f16 v[18:33], v[98:101], v[172:175], v[18:33]
	s_waitcnt lgkmcnt(3)
	v_mfma_f32_32x32x16_f16 v[18:33], v[94:97], v[176:179], v[18:33]
	s_waitcnt lgkmcnt(2)
	v_mfma_f32_32x32x16_f16 v[18:33], v[90:93], v[180:183], v[18:33]
	s_waitcnt lgkmcnt(1)
	v_mfma_f32_32x32x16_f16 v[18:33], v[86:89], v[184:187], v[18:33]
	s_waitcnt lgkmcnt(0)
	v_mfma_f32_32x32x16_f16 v[18:33], v[82:85], v[188:191], v[18:33]
	v_mov_b32_e32 v49, v17
	v_mov_b32_e32 v48, v16
	v_mov_b32_e32 v47, v15
	v_mov_b32_e32 v46, v14
	v_mov_b32_e32 v45, v13
	v_mov_b32_e32 v44, v12
	v_mov_b32_e32 v43, v11
	v_mov_b32_e32 v42, v10
	v_mov_b32_e32 v41, v9
	v_mov_b32_e32 v40, v8
	v_mov_b32_e32 v39, v7
	v_mov_b32_e32 v38, v6
	v_mov_b32_e32 v37, v5
	v_mov_b32_e32 v36, v4
	v_mov_b32_e32 v35, v3
	v_mov_b32_e32 v34, v2
